# k_g with the MLA all-ones B operand moved from v[196:203] to v[204:211] (v202/v203 are live clamp constants of the chunk-attention bias lookup; fixes a register clobber)
# speedup vs baseline: 1.0033x; 1.0025x over previous
; #define ALAS __attribute__((address_space(3)))
; #define ATT_WAIT_BAR() asm volatile("s_waitcnt vmcnt(0) lgkmcnt(0)\n\ts_barrier" ::: "memory")
; #define MF_ISSUE_K(t, s) do { glds16(ksrc + (long)(t) * 64 * 512, (unsigned)__builtin_amdgcn_readfirstlane(kdst + (s) * KSLOT)); \
;         if (wid < 4) glds16(krsrc + (long)(t) * 64 * 32, (unsigned)__builtin_amdgcn_readfirstlane(krdst + (s) * KSLOT)); } while (0)
; #define MF_ISSUE_V(t, s) glds16(vsrc + (long)(t) * 64 * 512, (unsigned)__builtin_amdgcn_readfirstlane(vdst + (s) * VSLOT))
; __device__ __forceinline__ bool mla_unit_fast88(const Args& A, int b, int h, int qb, ALAS char* shm, const int tidb) {
;     ...
;     MF_ISSUE_K(0, 0); MF_ISSUE_V(0, 0); MF_ISSUE_K(1, 1);
;     const unsigned char* Q8w = A.Q8 + (rowbase + q0 + wid * 32 + r32) * 768 + h * 96;
;     const unsigned char* Q8r = hi == 0 ? Q8w + 64 : A.ZERO;
;     v8i qf0, qf1;
;     { const u32x4 a0 = *(const u32x4*)(Q8w + 32 * hi), a1 = *(const u32x4*)(Q8w + 32 * hi + 16), b0 = *(const u32x4*)(Q8r), b1 = *(const u32x4*)(Q8r + 16);
;       qf0 = (v8i){(int)a0.x, (int)a0.y, (int)a0.z, (int)a0.w, (int)a1.x, (int)a1.y, (int)a1.z, (int)a1.w}; qf1 = (v8i){(int)b0.x, (int)b0.y, (int)b0.z, (int)b0.w, (int)b1.x, (int)b1.y, (int)b1.z, (int)b1.w}; }
;     const int sa8 = 0x7c7c7c7c, sb8 = 0x7b7b7b7b;
;     f32x16 o0 = {}, o1 = {}, ls = {};
;     const v8i ones8 = {0x38383838, 0x38383838, 0x38383838, 0x38383838, 0x38383838, 0x38383838, 0x38383838, 0x38383838};
;     const int vbo = ((lane >> 4) & 1) * 32 + (lane & 3) * 8 + (4 * hi + ((lane & 15) >> 2)) * 64;
;     ALAS const char* Kfr = shm + L_K + lane * 16;
;     ...
;     ATT_WAIT_BAR();
;     f32x16 cs[2][2];
;     { f32x16 z0 = {}, z1 = {}; ALAS const char* Ks_ = Kfr;
;       v8i k00, k01, k10, k11; M8_KFRAG(k00, Ks_, 0, 0); M8_KFRAG(k01, Ks_, 0, 1); M8_KFRAG(k10, Ks_, 1, 0); M8_KFRAG(k11, Ks_, 1, 1);
;       mfma8_acc(z0, k00, qf0, sa8, sb8); mfma8_acc(z1, k01, qf0, sa8, sb8); mfma8_acc(z0, k10, qf1, sa8, sb8); mfma8_acc(z1, k11, qf1, sa8, sb8);
;       asm volatile("s_nop 15\n\ts_nop 7" : "+v"(z0), "+v"(z1));
;       cs[0][0] = z0; cs[0][1] = z1; }
;     const float mhat = MF_ROWMAX(cs[0][0], cs[0][1]);
; #pragma unroll
;     for (int r = 0; r < 16; ++r) { cs[0][0][r] -= mhat; cs[0][1][r] -= mhat; }
;     f32x16 negm;
; #pragma unroll
;     for (int r = 0; r < 16; ++r) negm[r] = -mhat;
.LBB0_648:
	v_cmp_gt_u32_e32 vcc, 32, v154
	v_mov_b32_e32 v2, 0x800
	v_mov_b32_e32 v3, 0x8000
	v_cndmask_b32_e32 v2, 0, v2, vcc
	v_cndmask_b32_e64 v100, v2, v3, s[2:3]
	s_lshl_b32 s2, s6, 8
	v_mov_b32_e32 v101, v1
	s_lshl_b32 s37, s6, 2
	s_add_i32 s3, s45, 0x2000
	s_or_b32 s36, s30, s2
	s_lshl_b32 s2, s1, 5
	s_add_i32 s0, s37, 4
	s_add_i32 s47, s47, s37
	v_lshl_add_u64 v[2:3], v[146:147], 0, v[100:101]
	s_mov_b32 s4, m0
	s_mov_b32 m0, s3
	s_nop 0
	global_load_lds_dwordx4 v[2:3], off
	s_mov_b32 m0, s4
	s_ashr_i32 s3, s2, 31
	s_add_u32 s24, s36, s2
	v_or_b32_e32 v4, s24, v156
	v_mov_b64_e32 v[2:3], s[74:75]
	s_addc_u32 s25, s31, s3
	v_mad_u64_u32 v[2:3], s[2:3], v4, s67, v[2:3]
	v_mov_b32_e32 v4, 0x300
	v_mad_i32_i24 v3, s25, v4, v3
	v_lshl_add_u64 v[4:5], v[2:3], 0, 64
	v_mov_b32_e32 v6, s27
	v_cndmask_b32_e32 v5, v6, v5, vcc
	v_mov_b32_e32 v6, s26
	v_lshl_add_u64 v[2:3], v[2:3], 0, v[0:1]
	v_cndmask_b32_e32 v4, v6, v4, vcc
	global_load_dwordx4 v[134:137], v[2:3], off offset:16
	global_load_dwordx4 v[130:133], v[2:3], off
	global_load_dwordx4 v[142:145], v[4:5], off offset:16
	global_load_dwordx4 v[138:141], v[4:5], off
	v_lshlrev_b32_e32 v155, 4, v154
	s_mov_b32 s4, 0
	v_add_u32_e32 v157, 0, v155
	s_waitcnt vmcnt(0) lgkmcnt(0)
	s_barrier
	s_mov_b32 s18, s4
	s_mov_b32 s19, s4
	ds_read_b128 v[50:53], v157
	ds_read_b128 v[54:57], v157 offset:1024
	ds_read_b128 v[58:61], v157 offset:2048
	ds_read_b128 v[62:65], v157 offset:3072
	ds_read_b128 v[66:69], v157 offset:4096
	ds_read_b128 v[70:73], v157 offset:5120
	ds_read_b128 v[74:77], v157 offset:6144
	ds_read_b128 v[78:81], v157 offset:7168
	s_mov_b32 s5, s4
	s_mov_b32 s6, s4
	s_mov_b32 s7, s4
	s_mov_b32 s8, s4
	s_mov_b32 s9, s4
	s_mov_b32 s10, s4
	s_mov_b32 s11, s4
	s_mov_b32 s12, s4
	s_mov_b32 s13, s4
	s_mov_b32 s14, s4
	s_mov_b32 s15, s4
	s_mov_b32 s16, s4
	s_mov_b32 s17, s4
	v_mov_b64_e32 v[32:33], s[18:19]
	v_mov_b64_e32 v[30:31], s[16:17]
	v_mov_b64_e32 v[28:29], s[14:15]
	v_mov_b64_e32 v[26:27], s[12:13]
	v_mov_b64_e32 v[24:25], s[10:11]
	v_mov_b64_e32 v[22:23], s[8:9]
	v_mov_b64_e32 v[20:21], s[6:7]
	v_mov_b64_e32 v[18:19], s[4:5]
	v_mov_b64_e32 v[48:49], v[32:33]
	v_mov_b64_e32 v[46:47], v[30:31]
	v_mov_b64_e32 v[44:45], v[28:29]
	v_mov_b64_e32 v[42:43], v[26:27]
	v_mov_b64_e32 v[40:41], v[24:25]
	v_mov_b64_e32 v[38:39], v[22:23]
	v_mov_b64_e32 v[36:37], v[20:21]
	v_mov_b64_e32 v[34:35], v[18:19]
	v_mov_b32_e32 v16, v1
	v_mov_b32_e32 v17, v1
	v_mov_b32_e32 v2, v1
	v_mov_b32_e32 v3, v1
	v_mov_b32_e32 v4, v1
	v_mov_b32_e32 v5, v1
	v_mov_b32_e32 v6, v1
	v_mov_b32_e32 v7, v1
	v_mov_b32_e32 v8, v1
	v_mov_b32_e32 v9, v1
	v_mov_b32_e32 v10, v1
	v_mov_b32_e32 v11, v1
	v_mov_b32_e32 v12, v1
	v_mov_b32_e32 v13, v1
	v_mov_b32_e32 v14, v1
	v_mov_b32_e32 v15, v1
	s_mov_b32 s41, s31
	s_mov_b32 s5, 3
	v_mul_hi_u32_u24_e32 v149, 3, v100
	v_mul_u32_u24_e32 v148, 3, v100
	v_lshl_add_u64 v[150:151], v[98:99], 0, s[78:79]
	s_waitcnt vmcnt(0) lgkmcnt(0)
	v_mfma_scale_f32_32x32x64_f8f6f4 v[34:49], v[50:57], v[130:137], v[34:49], v247, v253 op_sel_hi:[0,0,0]
	s_waitcnt lgkmcnt(4)
	v_mfma_scale_f32_32x32x64_f8f6f4 v[18:33], v[58:65], v[130:137], v[18:33], v247, v253 op_sel_hi:[0,0,0]
	s_waitcnt vmcnt(0) lgkmcnt(2)
	v_mfma_scale_f32_32x32x64_f8f6f4 v[34:49], v[66:73], v[138:145], v[34:49], v247, v253 op_sel_hi:[0,0,0]
	s_waitcnt lgkmcnt(0)
	v_mfma_scale_f32_32x32x64_f8f6f4 v[18:33], v[74:81], v[138:145], v[18:33], v247, v253 op_sel_hi:[0,0,0]
	s_nop 0
	s_nop 15
	s_nop 7
	s_nop 0
	v_max3_f32 v0, v34, v18, v38
	s_nop 0
	v_max3_f32 v0, v0, v22, v42
	s_nop 0
	v_max3_f32 v0, v0, v26, v46
	s_nop 0
	v_max_f32_e32 v0, v0, v30
	v_max3_f32 v50, v35, v19, v39
	s_nop 0
	v_max3_f32 v50, v50, v23, v43
	s_nop 0
	v_max3_f32 v50, v50, v27, v47
	s_nop 0
	v_max_f32_e32 v50, v50, v31
	v_max3_f32 v51, v36, v20, v40
	s_nop 0
	v_max3_f32 v51, v51, v24, v44
	s_nop 0
	v_max3_f32 v51, v51, v28, v48
	s_nop 0
	v_max_f32_e32 v51, v51, v32
	v_max3_f32 v52, v37, v21, v41
	s_nop 0
	v_max3_f32 v52, v52, v25, v45
	s_nop 0
	v_max3_f32 v52, v52, v29, v49
	s_nop 0
	v_max_f32_e32 v52, v52, v33
	v_max3_f32 v0, v0, v50, v51
	s_nop 0
	v_max_f32_e32 v0, v0, v52
	s_nop 0
	v_mov_b32_e32 v50, v0
	s_nop 1
	v_permlane32_swap_b32_e32 v0, v50
	v_max_f32_e32 v50, v50, v50
	v_max_f32_e32 v0, v0, v0
	v_max_f32_e32 v0, v0, v50
	v_sub_f32_e32 v65, v49, v0
	v_sub_f32_e32 v64, v48, v0
	v_sub_f32_e32 v63, v47, v0
	v_sub_f32_e32 v62, v46, v0
	v_sub_f32_e32 v61, v45, v0
	v_sub_f32_e32 v60, v44, v0
	v_sub_f32_e32 v59, v43, v0
	v_sub_f32_e32 v58, v42, v0
	v_sub_f32_e32 v57, v41, v0
	v_sub_f32_e32 v56, v40, v0
	v_sub_f32_e32 v55, v39, v0
	v_sub_f32_e32 v54, v38, v0
	v_sub_f32_e32 v53, v37, v0
	v_sub_f32_e32 v52, v36, v0
	v_sub_f32_e32 v51, v35, v0
	v_sub_f32_e32 v50, v34, v0
	v_sub_f32_e32 v97, v33, v0
	v_sub_f32_e32 v96, v32, v0
	v_sub_f32_e32 v95, v31, v0
	v_sub_f32_e32 v94, v30, v0
	v_sub_f32_e32 v93, v29, v0
	v_sub_f32_e32 v92, v28, v0
	v_sub_f32_e32 v91, v27, v0
	v_sub_f32_e32 v90, v26, v0
	v_sub_f32_e32 v89, v25, v0
	v_sub_f32_e32 v88, v24, v0
	v_sub_f32_e32 v87, v23, v0
	v_sub_f32_e32 v86, v22, v0
	v_sub_f32_e32 v85, v21, v0
	v_sub_f32_e32 v84, v20, v0
	v_sub_f32_e32 v83, v19, v0
	v_sub_f32_e32 v82, v18, v0
	v_xor_b32_e32 v66, 0x80000000, v0
	v_mov_b64_e32 v[32:33], v[16:17]
	v_mov_b64_e32 v[48:49], v[16:17]
	v_mov_b32_e32 v67, v66
	v_mov_b32_e32 v68, v66
	v_mov_b32_e32 v69, v66
	v_mov_b32_e32 v70, v66
	v_mov_b32_e32 v71, v66
	v_mov_b32_e32 v72, v66
	v_mov_b32_e32 v73, v66
	v_mov_b32_e32 v74, v66
	v_mov_b32_e32 v75, v66
	v_mov_b32_e32 v76, v66
	v_mov_b32_e32 v77, v66
	v_mov_b32_e32 v78, v66
	v_mov_b32_e32 v79, v66
	v_mov_b32_e32 v80, v66
	v_mov_b32_e32 v81, v66
	v_lshlrev_b32_e32 v0, 1, v100
	v_mov_b64_e32 v[30:31], v[14:15]
	v_mov_b64_e32 v[28:29], v[12:13]
	v_mov_b64_e32 v[26:27], v[10:11]
	v_mov_b64_e32 v[24:25], v[8:9]
	v_mov_b64_e32 v[22:23], v[6:7]
	v_mov_b64_e32 v[20:21], v[4:5]
	v_mov_b64_e32 v[18:19], v[2:3]
	v_mov_b64_e32 v[46:47], v[14:15]
	v_mov_b64_e32 v[44:45], v[12:13]
	v_mov_b64_e32 v[42:43], v[10:11]
	v_mov_b64_e32 v[40:41], v[8:9]
	v_mov_b64_e32 v[38:39], v[6:7]
	v_mov_b64_e32 v[36:37], v[4:5]
	v_mov_b64_e32 v[34:35], v[2:3]
	v_mov_b32_e32 v172, 0
	v_mov_b32_e32 v173, 0
	v_mov_b32_e32 v174, 0
	v_mov_b32_e32 v175, 0
	v_mov_b32_e32 v176, 0
	v_mov_b32_e32 v177, 0
	v_mov_b32_e32 v178, 0
	v_mov_b32_e32 v179, 0
	v_mov_b32_e32 v180, 0
	v_mov_b32_e32 v181, 0
	v_mov_b32_e32 v182, 0
	v_mov_b32_e32 v183, 0
	v_mov_b32_e32 v184, 0
	v_mov_b32_e32 v185, 0
	v_mov_b32_e32 v186, 0
	v_mov_b32_e32 v187, 0
	v_mov_b32_e32 v204, v162
	v_mov_b32_e32 v205, v162
	v_mov_b32_e32 v206, v162
	v_mov_b32_e32 v207, v162
	v_mov_b32_e32 v208, v162
	v_mov_b32_e32 v209, v162
	v_mov_b32_e32 v210, v162
	v_mov_b32_e32 v211, v162

; #define ALAS __attribute__((address_space(3)))
; __device__ __forceinline__ bool mla_unit_fast88(const Args& A, int b, int h, int qb, ALAS char* shm, const int tidb) {
;     ...
;             if (vis) {
;                 {
;                     ALAS const char* Ks_ = Kfr + ks1 * KSLOT;
;                     v8i kfa, kfb; M8_KFRAG(kfa, Ks_, 0, 0);
;                     M8_KFRAG(kfb, Ks_, 0, 1);
;                     mfma8_new(N0, kfa, qf0, negm, sa8, sb8);
; #pragma unroll
;                     for (int e = 0; e < 8; ++e) C0[e] = __builtin_amdgcn_exp2f(C0[e]);
;                     __builtin_amdgcn_sched_barrier(0);
;                     M8_KFRAG(kfa, Ks_, 1, 0);
;                     mfma8_new(N1, kfb, qf0, negm, sa8, sb8);
; #pragma unroll
;                     for (int e = 8; e < 16; ++e) C0[e] = __builtin_amdgcn_exp2f(C0[e]);
;                     __builtin_amdgcn_sched_barrier(0);
;                     M8_KFRAG(kfb, Ks_, 1, 1);
;                     mfma8_acc(N0, kfa, qf1, sa8, sb8);
; #pragma unroll
;                     for (int e = 0; e < 8; ++e) C1[e] = __builtin_amdgcn_exp2f(C1[e]);
;                     __builtin_amdgcn_sched_barrier(0);
;                     mfma8_acc(N1, kfb, qf1, sa8, sb8);
; #pragma unroll
;                     for (int e = 8; e < 16; ++e) C1[e] = __builtin_amdgcn_exp2f(C1[e]);
;                     __builtin_amdgcn_sched_barrier(0);
;                 }
;                 ALAS const char* vb_ = shm + L_V + vs * 4096 + lane * 16;
;                 v8i vf0, vf1;
;                 { const u32x4 a0 = *(ALAS const u32x4*)(vb_), a1 = *(ALAS const u32x4*)(vb_ + 1024), b0 = *(ALAS const u32x4*)(vb_ + 2048), b1 = *(ALAS const u32x4*)(vb_ + 3072);
;                   vf0 = (v8i){(int)a0.x, (int)a0.y, (int)a0.z, (int)a0.w, (int)a1.x, (int)a1.y, (int)a1.z, (int)a1.w}; vf1 = (v8i){(int)b0.x, (int)b0.y, (int)b0.z, (int)b0.w, (int)b1.x, (int)b1.y, (int)b1.z, (int)b1.w}; }
;                 v8i pf;
; #pragma unroll
;                 for (int kk = 0; kk < 4; ++kk) { const f32x16& cc_ = (kk < 2) ? C0 : C1; const int k8_ = 8 * (kk & 1);
;                     int w0_ = 0, w1_ = 0;
;                     w0_ = __builtin_amdgcn_cvt_pk_bf8_f32(cc_[k8_], cc_[k8_ + 1], w0_, false); w0_ = __builtin_amdgcn_cvt_pk_bf8_f32(cc_[k8_ + 2], cc_[k8_ + 3], w0_, true);
.LBB0_653:
	s_add_i32 s7, s5, -3
	s_cmp_gt_i32 s7, s47
	s_cbranch_scc1 .Lmla_nv0
	v_lshl_add_u32 v158, s4, 13, v157
	v_exp_f32_e32 v50, v50
	v_exp_f32_e32 v51, v51
	v_exp_f32_e32 v52, v52
	v_exp_f32_e32 v53, v53
	v_exp_f32_e32 v54, v54
	v_exp_f32_e32 v55, v55
	v_exp_f32_e32 v56, v56
	v_exp_f32_e32 v57, v57
	s_waitcnt lgkmcnt(2)
	v_mfma_scale_f32_32x32x64_f8f6f4 v[98:113], v[114:121], v[130:137], v[66:81], v247, v253 op_sel_hi:[0,0,0]
	ds_read_b128 v[172:175], v158 offset:4096
	ds_read_b128 v[176:179], v158 offset:5120
	v_exp_f32_e32 v58, v58
	v_exp_f32_e32 v59, v59
	v_exp_f32_e32 v60, v60
	v_exp_f32_e32 v61, v61
	v_exp_f32_e32 v62, v62
	v_exp_f32_e32 v63, v63
	v_exp_f32_e32 v64, v64
	v_exp_f32_e32 v65, v65
	s_waitcnt lgkmcnt(2)
	v_mfma_scale_f32_32x32x64_f8f6f4 v[114:129], v[164:171], v[130:137], v[66:81], v247, v253 op_sel_hi:[0,0,0]
	ds_read_b128 v[164:167], v158 offset:6144
	ds_read_b128 v[168:171], v158 offset:7168
	v_exp_f32_e32 v82, v82
	v_exp_f32_e32 v83, v83
	v_exp_f32_e32 v84, v84
	v_exp_f32_e32 v85, v85
	v_exp_f32_e32 v86, v86
	v_exp_f32_e32 v87, v87
	v_exp_f32_e32 v88, v88
	v_exp_f32_e32 v89, v89
	s_waitcnt lgkmcnt(2)
	v_mfma_scale_f32_32x32x64_f8f6f4 v[98:113], v[172:179], v[138:145], v[98:113], v247, v253 op_sel_hi:[0,0,0]
	v_exp_f32_e32 v90, v90
	v_exp_f32_e32 v91, v91
	v_exp_f32_e32 v92, v92
	v_exp_f32_e32 v93, v93
	v_exp_f32_e32 v94, v94
	v_exp_f32_e32 v95, v95
	v_exp_f32_e32 v96, v96
	v_exp_f32_e32 v97, v97
	s_waitcnt lgkmcnt(0)
	v_mfma_scale_f32_32x32x64_f8f6f4 v[114:129], v[164:171], v[138:145], v[114:129], v247, v253 op_sel_hi:[0,0,0]
	ds_read_b128 v[164:167], v157 offset:36864
	ds_read_b128 v[168:171], v157 offset:37888
	ds_read_b128 v[172:175], v157 offset:38912
	ds_read_b128 v[176:179], v157 offset:39936
	v_cvt_pk_bf8_f32 v180, v50, v51
	v_cvt_pk_bf8_f32 v181, v54, v55
	v_cvt_pk_bf8_f32 v182, v58, v59
	v_cvt_pk_bf8_f32 v183, v62, v63
	v_cvt_pk_bf8_f32 v184, v82, v83
	v_cvt_pk_bf8_f32 v185, v86, v87
	v_cvt_pk_bf8_f32 v186, v90, v91
	v_cvt_pk_bf8_f32 v187, v94, v95
	v_cvt_pk_bf8_f32 v180, v52, v53 op_sel:[0,0,1]
	v_cvt_pk_bf8_f32 v181, v56, v57 op_sel:[0,0,1]
	v_cvt_pk_bf8_f32 v182, v60, v61 op_sel:[0,0,1]
	v_cvt_pk_bf8_f32 v183, v64, v65 op_sel:[0,0,1]
	v_cvt_pk_bf8_f32 v184, v84, v85 op_sel:[0,0,1]
	v_cvt_pk_bf8_f32 v185, v88, v89 op_sel:[0,0,1]
	v_cvt_pk_bf8_f32 v186, v92, v93 op_sel:[0,0,1]
	v_cvt_pk_bf8_f32 v187, v96, v97 op_sel:[0,0,1]
	s_waitcnt lgkmcnt(2)
	v_mfma_scale_f32_32x32x64_f8f6f4 v[2:17], v[180:187], v[164:171], v[2:17], v251, v247 op_sel_hi:[0,0,0] cbsz:1
	s_waitcnt lgkmcnt(0)
	v_mfma_scale_f32_32x32x64_f8f6f4 v[34:49], v[180:187], v[204:211], v[34:49], v251, v251 op_sel_hi:[0,0,0] cbsz:1

; #define ALAS __attribute__((address_space(3)))
; __device__ __forceinline__ bool mla_unit_fast88(const Args& A, int b, int h, int qb, ALAS char* shm, const int tidb) {
;     ...
;             if (vis) {
;                 {
;                     ALAS const char* Ks_ = Kfr + ks1 * KSLOT;
;                     v8i kfa, kfb; M8_KFRAG(kfa, Ks_, 0, 0);
;                     M8_KFRAG(kfb, Ks_, 0, 1);
;                     mfma8_new(N0, kfa, qf0, negm, sa8, sb8);
; #pragma unroll
;                     for (int e = 0; e < 8; ++e) C0[e] = __builtin_amdgcn_exp2f(C0[e]);
;                     __builtin_amdgcn_sched_barrier(0);
;                     M8_KFRAG(kfa, Ks_, 1, 0);
;                     mfma8_new(N1, kfb, qf0, negm, sa8, sb8);
; #pragma unroll
;                     for (int e = 8; e < 16; ++e) C0[e] = __builtin_amdgcn_exp2f(C0[e]);
;                     __builtin_amdgcn_sched_barrier(0);
;                     M8_KFRAG(kfb, Ks_, 1, 1);
;                     mfma8_acc(N0, kfa, qf1, sa8, sb8);
; #pragma unroll
;                     for (int e = 0; e < 8; ++e) C1[e] = __builtin_amdgcn_exp2f(C1[e]);
;                     __builtin_amdgcn_sched_barrier(0);
;                     mfma8_acc(N1, kfb, qf1, sa8, sb8);
; #pragma unroll
;                     for (int e = 8; e < 16; ++e) C1[e] = __builtin_amdgcn_exp2f(C1[e]);
;                     __builtin_amdgcn_sched_barrier(0);
;                 }
;                 ALAS const char* vb_ = shm + L_V + vs * 4096 + lane * 16;
;                 v8i vf0, vf1;
;                 { const u32x4 a0 = *(ALAS const u32x4*)(vb_), a1 = *(ALAS const u32x4*)(vb_ + 1024), b0 = *(ALAS const u32x4*)(vb_ + 2048), b1 = *(ALAS const u32x4*)(vb_ + 3072);
;                   vf0 = (v8i){(int)a0.x, (int)a0.y, (int)a0.z, (int)a0.w, (int)a1.x, (int)a1.y, (int)a1.z, (int)a1.w}; vf1 = (v8i){(int)b0.x, (int)b0.y, (int)b0.z, (int)b0.w, (int)b1.x, (int)b1.y, (int)b1.z, (int)b1.w}; }
;                 v8i pf;
; #pragma unroll
;                 for (int kk = 0; kk < 4; ++kk) { const f32x16& cc_ = (kk < 2) ? C0 : C1; const int k8_ = 8 * (kk & 1);
;                     int w0_ = 0, w1_ = 0;
;                     w0_ = __builtin_amdgcn_cvt_pk_bf8_f32(cc_[k8_], cc_[k8_ + 1], w0_, false); w0_ = __builtin_amdgcn_cvt_pk_bf8_f32(cc_[k8_ + 2], cc_[k8_ + 3], w0_, true);
.LBB0_658:
	v_lshl_add_u32 v146, s4, 13, v157
	v_exp_f32_e32 v98, v98
	v_exp_f32_e32 v99, v99
	v_exp_f32_e32 v100, v100
	v_exp_f32_e32 v101, v101
	v_exp_f32_e32 v102, v102
	v_exp_f32_e32 v103, v103
	v_exp_f32_e32 v104, v104
	v_exp_f32_e32 v105, v105
	s_waitcnt lgkmcnt(2)
	v_mfma_scale_f32_32x32x64_f8f6f4 v[50:65], v[82:89], v[130:137], v[66:81], v247, v253 op_sel_hi:[0,0,0]
	ds_read_b128 v[172:175], v146 offset:4096
	ds_read_b128 v[176:179], v146 offset:5120
	v_exp_f32_e32 v106, v106
	v_exp_f32_e32 v107, v107
	v_exp_f32_e32 v108, v108
	v_exp_f32_e32 v109, v109
	v_exp_f32_e32 v110, v110
	v_exp_f32_e32 v111, v111
	v_exp_f32_e32 v112, v112
	v_exp_f32_e32 v113, v113
	s_waitcnt lgkmcnt(2)
	v_mfma_scale_f32_32x32x64_f8f6f4 v[82:97], v[164:171], v[130:137], v[66:81], v247, v253 op_sel_hi:[0,0,0]
	ds_read_b128 v[164:167], v146 offset:6144
	ds_read_b128 v[168:171], v146 offset:7168
	v_exp_f32_e32 v114, v114
	v_exp_f32_e32 v115, v115
	v_exp_f32_e32 v116, v116
	v_exp_f32_e32 v117, v117
	v_exp_f32_e32 v118, v118
	v_exp_f32_e32 v119, v119
	v_exp_f32_e32 v120, v120
	v_exp_f32_e32 v121, v121
	s_waitcnt lgkmcnt(2)
	v_mfma_scale_f32_32x32x64_f8f6f4 v[50:65], v[172:179], v[138:145], v[50:65], v247, v253 op_sel_hi:[0,0,0]
	v_exp_f32_e32 v122, v122
	v_exp_f32_e32 v123, v123
	v_exp_f32_e32 v124, v124
	v_exp_f32_e32 v125, v125
	v_exp_f32_e32 v126, v126
	v_exp_f32_e32 v127, v127
	v_exp_f32_e32 v128, v128
	v_exp_f32_e32 v129, v129
	s_waitcnt lgkmcnt(0)
	v_mfma_scale_f32_32x32x64_f8f6f4 v[82:97], v[164:171], v[138:145], v[82:97], v247, v253 op_sel_hi:[0,0,0]
	ds_read_b128 v[164:167], v157 offset:40960
	ds_read_b128 v[168:171], v157 offset:41984
	ds_read_b128 v[172:175], v157 offset:43008
	ds_read_b128 v[176:179], v157 offset:44032
	v_cvt_pk_bf8_f32 v180, v98, v99
	v_cvt_pk_bf8_f32 v181, v102, v103
	v_cvt_pk_bf8_f32 v182, v106, v107
	v_cvt_pk_bf8_f32 v183, v110, v111
	v_cvt_pk_bf8_f32 v184, v114, v115
	v_cvt_pk_bf8_f32 v185, v118, v119
	v_cvt_pk_bf8_f32 v186, v122, v123
	v_cvt_pk_bf8_f32 v187, v126, v127
	v_cvt_pk_bf8_f32 v180, v100, v101 op_sel:[0,0,1]
	v_cvt_pk_bf8_f32 v181, v104, v105 op_sel:[0,0,1]
	v_cvt_pk_bf8_f32 v182, v108, v109 op_sel:[0,0,1]
	v_cvt_pk_bf8_f32 v183, v112, v113 op_sel:[0,0,1]
	v_cvt_pk_bf8_f32 v184, v116, v117 op_sel:[0,0,1]
	v_cvt_pk_bf8_f32 v185, v120, v121 op_sel:[0,0,1]
	v_cvt_pk_bf8_f32 v186, v124, v125 op_sel:[0,0,1]
	v_cvt_pk_bf8_f32 v187, v128, v129 op_sel:[0,0,1]
	s_waitcnt lgkmcnt(2)
	v_mfma_scale_f32_32x32x64_f8f6f4 v[2:17], v[180:187], v[164:171], v[2:17], v251, v247 op_sel_hi:[0,0,0] cbsz:1
	s_waitcnt lgkmcnt(0)
	v_mfma_scale_f32_32x32x64_f8f6f4 v[34:49], v[180:187], v[204:211], v[34:49], v251, v251 op_sel_hi:[0,0,0] cbsz:1
